# c31: c29 + class-2 MoE weight conversion moved from after the layer-0 down-projection GEMM to before the out-projection (no conversion traffic overlaps any D0 GEMM)
# baseline (speedup 1.0000x reference)
; __global__ void __launch_bounds__(NTHREADS, 2) fwd(Args args) {
;     ...
;     if (IN(PH_OUT0)) {
;         pg8::Gemm g{CAT0, (const bf16*)(ws + WS_WOUT0), SEQ, DM, DM, 0}; pg8::StaticOrder S; S.init(SEQ, DM, GRID, F.bid);
;         pg8::EpiResF32 E{nullptr, HN, nullptr, DM, HN, SS0, MISC_OFF + 1024};
;         pg8::gemm_phase<pg8::EpiResF32, pg8::StaticOrder, true, true>(F.lds + RING_OFF, g, S, E);
;     ...
;         if (conv_cls == 1) { moe_deep_items(args.in[18], args.in[19], args.in[20], ws, FILL1 + FILL2, MOE_ITEMS, gw, NGW, cscr, F.lane); __syncthreads(); }
;         pg8::gemm_phase<pg8::EpiResF32, pg8::StaticOrder, true, true>(F.lds + RING_OFF, g, S, E);
;         if (conv_cls == 2) { moe_deep_items(args.in[18], args.in[19], args.in[20], ws, FILL1 + FILL2, MOE_ITEMS, gw, NGW, cscr, F.lane); __syncthreads(); }
.LBB0_418:
	s_cmp_lt_i32 s64, 4
	s_cselect_b64 s[4:5], -1, 0
	s_and_b64 s[16:17], s[4:5], s[8:9]
	s_mov_b32 s98, 0
	s_andn2_b64 vcc, exec, s[16:17]
	s_cbranch_vccnz .LBB0_463
	s_mul_i32 s0, s67, 0x56
	s_lshr_b32 s0, s0, 8
	s_mul_i32 s0, s0, 3
	s_sub_i32 s0, s67, s0
	s_cmp_lg_u32 s0, 2
	s_cbranch_scc1 .Lout0_body
	s_mov_b64 s[100:101], s[16:17]
	v_readlane_b32 s82, v248, 9
	s_mov_b32 s98, 2
	s_nop 1
	s_lshl_b32 s72, s82, 14
	s_branch .Lconv2_entry
.Lout0_body:
	s_waitcnt vmcnt(0)
	v_mov_b32_e32 v2, v0
	s_cmpk_lt_i32 s2, 0x100
	s_cselect_b64 s[8:9], -1, 0
	s_cmpk_gt_i32 s2, 0xff
	v_readfirstlane_b32 s3, v2
	s_cbranch_scc1 .LBB0_425
	s_ashr_i32 s0, s2, 31
	s_lshr_b32 s0, s0, 29
	s_add_i32 s4, s2, s0
	s_and_b32 s0, s4, -8
	s_sub_i32 s5, s2, s0
	s_cmp_gt_i32 s5, -1
	s_cbranch_scc0 .LBB0_422
	s_lshl_b32 s6, s5, 5
	s_cbranch_execz .LBB0_423
	s_branch .LBB0_424
.LBB0_422:
.LBB0_423:
	s_mul_i32 s6, s5, 33

; __global__ void __launch_bounds__(NTHREADS, 2) fwd(Args args) {
;     ...
;         if (conv_cls == 2) { moe_deep_items(args.in[18], args.in[19], args.in[20], ws, FILL1 + FILL2, MOE_ITEMS, gw, NGW, cscr, F.lane); __syncthreads(); }
.LBB0_704:
	s_cmp_eq_u32 s98, 3
	s_cbranch_scc1 .LBB0_767

; __global__ void __launch_bounds__(NTHREADS, 2) fwd(Args args) {
;     ...
;         if (conv_cls == 2) { moe_deep_items(args.in[18], args.in[19], args.in[20], ws, FILL1 + FILL2, MOE_ITEMS, gw, NGW, cscr, F.lane); __syncthreads(); }
.LBB0_766:
	s_waitcnt vmcnt(0) lgkmcnt(0)
	s_barrier
	s_cmp_eq_u32 s98, 2
	s_cbranch_scc0 .LBB0_767
	s_mov_b32 s98, 3
	s_mov_b64 s[16:17], s[100:101]
	s_waitcnt lgkmcnt(0)
	s_barrier
	s_branch .Lout0_body

; __global__ void __launch_bounds__(NTHREADS, 2) fwd(Args args) {
	.amdhsa_kernel _Z3fwd4Args
		.amdhsa_group_segment_fixed_size 0
		.amdhsa_private_segment_fixed_size 0
		.amdhsa_kernarg_size 448
		.amdhsa_user_sgpr_count 2
		.amdhsa_user_sgpr_dispatch_ptr 0
		.amdhsa_user_sgpr_queue_ptr 0
		.amdhsa_user_sgpr_kernarg_segment_ptr 1
		.amdhsa_user_sgpr_dispatch_id 0
		.amdhsa_user_sgpr_kernarg_preload_length 0
		.amdhsa_user_sgpr_kernarg_preload_offset 0
		.amdhsa_user_sgpr_private_segment_size 0
		.amdhsa_uses_dynamic_stack 0
		.amdhsa_enable_private_segment 0
		.amdhsa_system_sgpr_workgroup_id_x 1
		.amdhsa_system_sgpr_workgroup_id_y 0
		.amdhsa_system_sgpr_workgroup_id_z 0
		.amdhsa_system_sgpr_workgroup_info 0
		.amdhsa_system_vgpr_workitem_id 0
		.amdhsa_next_free_vgpr 249
		.amdhsa_next_free_sgpr 102
		.amdhsa_accum_offset 252
		.amdhsa_reserve_vcc 1
		.amdhsa_float_round_mode_32 0
		.amdhsa_float_round_mode_16_64 0
		.amdhsa_float_denorm_mode_32 3
		.amdhsa_float_denorm_mode_16_64 3
		.amdhsa_dx10_clamp 1
		.amdhsa_ieee_mode 1
		.amdhsa_fp16_overflow 0
		.amdhsa_tg_split 0
		.amdhsa_exception_fp_ieee_invalid_op 0
		.amdhsa_exception_fp_denorm_src 0
		.amdhsa_exception_fp_ieee_div_zero 0
		.amdhsa_exception_fp_ieee_overflow 0
		.amdhsa_exception_fp_ieee_underflow 0
		.amdhsa_exception_fp_ieee_inexact 0
		.amdhsa_exception_int_div_zero 0
	.end_amdhsa_kernel

; __global__ void __launch_bounds__(NTHREADS, 2) fwd(Args args) {
amdhsa.kernels:
  - .agpr_count:     0
    .args:
      - .offset:         0
        .size:           192
        .value_kind:     by_value
      - .offset:         192
        .size:           4
        .value_kind:     hidden_block_count_x
      - .offset:         196
        .size:           4
        .value_kind:     hidden_block_count_y
      - .offset:         200
        .size:           4
        .value_kind:     hidden_block_count_z
      - .offset:         204
        .size:           2
        .value_kind:     hidden_group_size_x
      - .offset:         206
        .size:           2
        .value_kind:     hidden_group_size_y
      - .offset:         208
        .size:           2
        .value_kind:     hidden_group_size_z
      - .offset:         210
        .size:           2
        .value_kind:     hidden_remainder_x
      - .offset:         212
        .size:           2
        .value_kind:     hidden_remainder_y
      - .offset:         214
        .size:           2
        .value_kind:     hidden_remainder_z
      - .offset:         232
        .size:           8
        .value_kind:     hidden_global_offset_x
      - .offset:         240
        .size:           8
        .value_kind:     hidden_global_offset_y
      - .offset:         248
        .size:           8
        .value_kind:     hidden_global_offset_z
      - .offset:         256
        .size:           2
        .value_kind:     hidden_grid_dims
      - .offset:         312
        .size:           4
        .value_kind:     hidden_dynamic_lds_size
    .group_segment_fixed_size: 0
    .kernarg_segment_align: 8
    .kernarg_segment_size: 448
    .language:       OpenCL C
    .language_version:
      - 2
      - 0
    .max_flat_workgroup_size: 512
    .name:           _Z3fwd4Args
    .private_segment_fixed_size: 0
    .sgpr_count:     108
    .sgpr_spill_count: 10
    .symbol:         _Z3fwd4Args.kd
    .uniform_work_group_size: 1
    .uses_dynamic_stack: false
    .vgpr_count:     249
    .vgpr_spill_count: 0
    .wavefront_size: 64
